# speedup vs baseline: 1.0316x; 1.0308x over previous
.LBB8_12:
	ds_read_b128 v[146:149], v188
	ds_read_b128 v[150:153], v188 offset:1024
	ds_read_b128 v[154:157], v188 offset:2048
	ds_read_b128 v[158:161], v188 offset:3072
	ds_read_b128 v[226:229], v190
	ds_read_b128 v[230:233], v190 offset:1024
	ds_read_b128 v[234:237], v190 offset:2048
	ds_read_b128 v[238:241], v190 offset:3072
	s_cmp_eq_u32 s51, s61
	s_cselect_b64 s[66:67], -1, 0
	s_add_i32 s61, s61, 2
	s_and_b64 s[34:35], s[66:67], exec
	s_cselect_b32 s35, s31, s60
	s_cselect_b32 s34, s30, s59
	s_cselect_b32 s64, s37, s57
	s_lshl_b32 s65, s64, 13
	s_and_b64 s[66:67], s[66:67], exec
	s_cselect_b32 s63, 0, s62
	s_add_i32 s68, s65, s63
	ds_read_b128 v[194:197], v189
	ds_read_b128 v[198:201], v189 offset:1024
	ds_read_b128 v[202:205], v189 offset:2048
	ds_read_b128 v[206:209], v189 offset:3072
	ds_read_b128 v[210:213], v189 offset:4096
	ds_read_b128 v[214:217], v189 offset:5120
	ds_read_b128 v[218:221], v189 offset:6144
	ds_read_b128 v[222:225], v189 offset:7168
	s_ashr_i32 s69, s68, 31
	s_waitcnt vmcnt(2)
	s_lshl_b64 s[66:67], s[68:69], 1
	v_pk_add_f16 v14, v14, v10
	v_pk_add_f16 v15, v15, v11
	v_pk_add_f16 v16, v16, v12
	v_pk_add_f16 v17, v17, v13
	s_add_u32 s70, s8, s66
	v_pk_max_f16 v17, v17, 0
	v_pk_max_f16 v16, v16, 0
	v_pk_max_f16 v15, v15, 0
	v_pk_max_f16 v14, v14, 0
	v_pk_add_f16 v6, v6, v10
	v_pk_add_f16 v7, v7, v11
	v_pk_add_f16 v8, v8, v12
	v_pk_add_f16 v9, v9, v13
	s_addc_u32 s71, s9, s67
	s_add_i32 s68, s68, s65
	v_pk_max_f16 v9, v9, 0
	v_pk_max_f16 v8, v8, 0
	v_pk_max_f16 v7, v7, 0
	v_pk_max_f16 v6, v6, 0
	ds_write_b128 v186, v[14:17] offset:49152
	ds_write_b128 v186, v[6:9] offset:57344
	s_ashr_i32 s69, s68, 31
	s_lshl_b32 s66, s64, 14
	s_lshl_b64 s[68:69], s[68:69], 1
	s_nop 4
	global_load_dwordx4 v[6:9], v184, s[70:71]
	s_add_u32 s68, s10, s68
	global_load_dwordx4 v[10:13], v185, s[70:71]
	s_addc_u32 s69, s11, s69
	global_load_dwordx4 v[14:17], v183, s[68:69]
	s_waitcnt lgkmcnt(8)
	s_barrier
	s_waitcnt lgkmcnt(0)
	s_setprio 1
	s_waitcnt lgkmcnt(0)
	v_mfma_f32_16x16x32_f16 v[138:141], v[146:149], v[194:197], v[138:141]
	v_mfma_f32_16x16x32_f16 v[142:145], v[154:157], v[194:197], v[142:145]
	v_mfma_f32_16x16x32_f16 v[126:129], v[146:149], v[202:205], v[126:129]
	v_mfma_f32_16x16x32_f16 v[122:125], v[154:157], v[202:205], v[122:125]
	v_mfma_f32_16x16x32_f16 v[110:113], v[146:149], v[210:213], v[110:113]
	v_mfma_f32_16x16x32_f16 v[106:109], v[154:157], v[210:213], v[106:109]
	v_mfma_f32_16x16x32_f16 v[94:97], v[146:149], v[218:221], v[94:97]
	v_mfma_f32_16x16x32_f16 v[90:93], v[154:157], v[218:221], v[90:93]
	v_mfma_f32_16x16x32_f16 v[138:141], v[150:153], v[198:201], v[138:141]
	v_mfma_f32_16x16x32_f16 v[142:145], v[158:161], v[198:201], v[142:145]
	v_mfma_f32_16x16x32_f16 v[126:129], v[150:153], v[206:209], v[126:129]
	v_mfma_f32_16x16x32_f16 v[122:125], v[158:161], v[206:209], v[122:125]
	v_mfma_f32_16x16x32_f16 v[110:113], v[150:153], v[214:217], v[110:113]
	v_mfma_f32_16x16x32_f16 v[106:109], v[158:161], v[214:217], v[106:109]
	v_mfma_f32_16x16x32_f16 v[94:97], v[150:153], v[222:225], v[94:97]
	v_mfma_f32_16x16x32_f16 v[90:93], v[158:161], v[222:225], v[90:93]
	s_setprio 0
	s_waitcnt lgkmcnt(0)
	s_setprio 1
	s_waitcnt lgkmcnt(0)
	v_mfma_f32_16x16x32_f16 v[134:137], v[226:229], v[194:197], v[134:137]
	v_mfma_f32_16x16x32_f16 v[130:133], v[234:237], v[194:197], v[130:133]
	v_mfma_f32_16x16x32_f16 v[118:121], v[226:229], v[202:205], v[118:121]
	v_mfma_f32_16x16x32_f16 v[114:117], v[234:237], v[202:205], v[114:117]
	v_mfma_f32_16x16x32_f16 v[102:105], v[226:229], v[210:213], v[102:105]
	v_mfma_f32_16x16x32_f16 v[98:101], v[234:237], v[210:213], v[98:101]
	v_mfma_f32_16x16x32_f16 v[86:89], v[226:229], v[218:221], v[86:89]
	v_mfma_f32_16x16x32_f16 v[82:85], v[234:237], v[218:221], v[82:85]
	v_mfma_f32_16x16x32_f16 v[134:137], v[230:233], v[198:201], v[134:137]
	v_mfma_f32_16x16x32_f16 v[130:133], v[238:241], v[198:201], v[130:133]
	v_mfma_f32_16x16x32_f16 v[118:121], v[230:233], v[206:209], v[118:121]
	v_mfma_f32_16x16x32_f16 v[114:117], v[238:241], v[206:209], v[114:117]
	v_mfma_f32_16x16x32_f16 v[102:105], v[230:233], v[214:217], v[102:105]
	v_mfma_f32_16x16x32_f16 v[98:101], v[238:241], v[214:217], v[98:101]
	v_mfma_f32_16x16x32_f16 v[86:89], v[230:233], v[222:225], v[86:89]
	v_mfma_f32_16x16x32_f16 v[82:85], v[238:241], v[222:225], v[82:85]
	s_setprio 0
	s_or_b32 s64, s65, 0x1000
	s_add_i32 s68, s64, s63
	s_barrier
	s_add_i32 s81, s53, s45
	v_lshl_add_u64 v[170:171], s[34:35], 0, v[162:163]
	s_mov_b32 m0, s81
	global_load_lds_dwordx4 v[170:171], off
	v_lshl_add_u64 v[242:243], s[34:35], 0, v[164:165]
	s_add_i32 m0, s81, 0x2000
	s_nop 0
	global_load_lds_dwordx4 v[242:243], off
	ds_read_b128 v[194:197], v189 offset:16384
	ds_read_b128 v[198:201], v189 offset:17408
	ds_read_b128 v[202:205], v189 offset:18432
	ds_read_b128 v[206:209], v189 offset:19456
	ds_read_b128 v[210:213], v189 offset:20480
	ds_read_b128 v[214:217], v189 offset:21504
	ds_read_b128 v[218:221], v189 offset:22528
	ds_read_b128 v[222:225], v189 offset:23552
	s_ashr_i32 s69, s68, 31
	s_lshl_b64 s[68:69], s[68:69], 1
	s_waitcnt vmcnt(2)
	s_add_u32 s68, s8, s68
	v_pk_add_f16 v6, v6, v14
	v_pk_add_f16 v7, v7, v15
	v_pk_add_f16 v8, v8, v16
	v_pk_add_f16 v9, v9, v17
	s_addc_u32 s69, s9, s69
	s_or_b32 s67, s66, 0x2000
	v_pk_max_f16 v9, v9, 0
	v_pk_max_f16 v8, v8, 0
	v_pk_max_f16 v7, v7, 0
	v_pk_max_f16 v6, v6, 0
	v_pk_add_f16 v10, v10, v14
	v_pk_add_f16 v11, v11, v15
	v_pk_add_f16 v12, v12, v16
	v_pk_add_f16 v13, v13, v17
	s_add_i32 s70, s67, s63
	v_pk_max_f16 v13, v13, 0
	v_pk_max_f16 v12, v12, 0
	v_pk_max_f16 v11, v11, 0
	v_pk_max_f16 v10, v10, 0
	ds_write_b128 v186, v[6:9]
	ds_write_b128 v186, v[10:13] offset:8192
	s_ashr_i32 s71, s70, 31
	s_lshl_b64 s[70:71], s[70:71], 1
	s_nop 4
	global_load_dwordx4 v[6:9], v184, s[68:69]
	s_add_u32 s70, s10, s70
	global_load_dwordx4 v[10:13], v185, s[68:69]
	s_addc_u32 s71, s11, s71
	global_load_dwordx4 v[14:17], v183, s[70:71]
	s_barrier
	s_waitcnt lgkmcnt(0)
	s_setprio 1
	s_waitcnt lgkmcnt(0)
	v_mfma_f32_16x16x32_f16 v[78:81], v[146:149], v[194:197], v[78:81]
	v_mfma_f32_16x16x32_f16 v[74:77], v[154:157], v[194:197], v[74:77]
	v_mfma_f32_16x16x32_f16 v[62:65], v[146:149], v[202:205], v[62:65]
	v_mfma_f32_16x16x32_f16 v[58:61], v[154:157], v[202:205], v[58:61]
	v_mfma_f32_16x16x32_f16 v[46:49], v[146:149], v[210:213], v[46:49]
	v_mfma_f32_16x16x32_f16 v[42:45], v[154:157], v[210:213], v[42:45]
	v_mfma_f32_16x16x32_f16 v[30:33], v[146:149], v[218:221], v[30:33]
	v_mfma_f32_16x16x32_f16 v[26:29], v[154:157], v[218:221], v[26:29]
	v_mfma_f32_16x16x32_f16 v[78:81], v[150:153], v[198:201], v[78:81]
	v_mfma_f32_16x16x32_f16 v[74:77], v[158:161], v[198:201], v[74:77]
	v_mfma_f32_16x16x32_f16 v[62:65], v[150:153], v[206:209], v[62:65]
	v_mfma_f32_16x16x32_f16 v[58:61], v[158:161], v[206:209], v[58:61]
	v_mfma_f32_16x16x32_f16 v[46:49], v[150:153], v[214:217], v[46:49]
	v_mfma_f32_16x16x32_f16 v[42:45], v[158:161], v[214:217], v[42:45]
	v_mfma_f32_16x16x32_f16 v[30:33], v[150:153], v[222:225], v[30:33]
	v_mfma_f32_16x16x32_f16 v[26:29], v[158:161], v[222:225], v[26:29]
	s_setprio 0
	s_barrier
	s_add_u32 s34, s34, s22
	s_addc_u32 s35, s35, s23
	s_add_i32 s68, s54, s45
	v_lshl_add_u64 v[244:245], s[34:35], 0, v[162:163]
	s_mov_b32 m0, s68
	v_lshl_add_u64 v[246:247], s[34:35], 0, v[164:165]
	global_load_lds_dwordx4 v[244:245], off
	s_add_i32 m0, s68, 0x2000
	s_nop 0
	global_load_lds_dwordx4 v[246:247], off
	s_waitcnt vmcnt(6)
	s_barrier
	s_setprio 1
	v_mfma_f32_16x16x32_f16 v[70:73], v[226:229], v[194:197], v[70:73]
	v_mfma_f32_16x16x32_f16 v[66:69], v[234:237], v[194:197], v[66:69]
	v_mfma_f32_16x16x32_f16 v[54:57], v[226:229], v[202:205], v[54:57]
	v_mfma_f32_16x16x32_f16 v[50:53], v[234:237], v[202:205], v[50:53]
	v_mfma_f32_16x16x32_f16 v[38:41], v[226:229], v[210:213], v[38:41]
	v_mfma_f32_16x16x32_f16 v[34:37], v[234:237], v[210:213], v[34:37]
	v_mfma_f32_16x16x32_f16 v[22:25], v[226:229], v[218:221], v[22:25]
	v_mfma_f32_16x16x32_f16 v[18:21], v[234:237], v[218:221], v[18:21]
	v_mfma_f32_16x16x32_f16 v[70:73], v[230:233], v[198:201], v[70:73]
	v_mfma_f32_16x16x32_f16 v[66:69], v[238:241], v[198:201], v[66:69]
	v_mfma_f32_16x16x32_f16 v[54:57], v[230:233], v[206:209], v[54:57]
	v_mfma_f32_16x16x32_f16 v[50:53], v[238:241], v[206:209], v[50:53]
	v_mfma_f32_16x16x32_f16 v[38:41], v[230:233], v[214:217], v[38:41]
	v_mfma_f32_16x16x32_f16 v[34:37], v[238:241], v[214:217], v[34:37]
	v_mfma_f32_16x16x32_f16 v[22:25], v[230:233], v[222:225], v[22:25]
	v_mfma_f32_16x16x32_f16 v[18:21], v[238:241], v[222:225], v[18:21]
	s_setprio 0
	s_barrier
	ds_read_b128 v[146:149], v191
	ds_read_b128 v[150:153], v191 offset:1024
	ds_read_b128 v[154:157], v191 offset:2048
	ds_read_b128 v[158:161], v191 offset:3072
	ds_read_b128 v[226:229], v192
	ds_read_b128 v[230:233], v192 offset:1024
	ds_read_b128 v[234:237], v192 offset:2048
	ds_read_b128 v[238:241], v192 offset:3072
	s_or_b32 s70, s63, 64
	s_ashr_i32 s35, s65, 31
	s_ashr_i32 s69, s63, 31
	s_add_u32 s34, s63, s65
	s_addc_u32 s35, s69, s35
	s_lshl_b64 s[34:35], s[34:35], 1
	s_add_u32 s34, s8, s34
	s_addc_u32 s35, s9, s35
	s_add_u32 s34, s34, 0x80
	ds_read_b128 v[194:197], v189 offset:32768
	ds_read_b128 v[198:201], v189 offset:33792
	ds_read_b128 v[202:205], v189 offset:34816
	ds_read_b128 v[206:209], v189 offset:35840
	ds_read_b128 v[210:213], v189 offset:36864
	ds_read_b128 v[214:217], v189 offset:37888
	ds_read_b128 v[218:221], v189 offset:38912
	ds_read_b128 v[222:225], v189 offset:39936
	s_addc_u32 s35, s35, 0
	s_ashr_i32 s65, s66, 31
	s_waitcnt vmcnt(2)
	s_add_u32 s68, s63, s66
	v_pk_add_f16 v6, v6, v14
	v_pk_add_f16 v7, v7, v15
	v_pk_add_f16 v8, v8, v16
	v_pk_add_f16 v9, v9, v17
	s_addc_u32 s69, s69, s65
	v_pk_max_f16 v9, v9, 0
	v_pk_max_f16 v8, v8, 0
	v_pk_max_f16 v7, v7, 0
	v_pk_max_f16 v6, v6, 0
	v_pk_add_f16 v10, v10, v14
	v_pk_add_f16 v11, v11, v15
	v_pk_add_f16 v12, v12, v16
	v_pk_add_f16 v13, v13, v17
	s_lshl_b64 s[68:69], s[68:69], 1
	v_pk_max_f16 v13, v13, 0
	v_pk_max_f16 v12, v12, 0
	v_pk_max_f16 v11, v11, 0
	v_pk_max_f16 v10, v10, 0
	ds_write_b128 v186, v[6:9] offset:16384
	ds_write_b128 v186, v[10:13] offset:24576
	s_add_u32 s63, s10, s68
	s_addc_u32 s65, s11, s69
	s_nop 4
	global_load_dwordx4 v[6:9], v184, s[34:35]
	s_add_u32 s68, s63, 0x80
	global_load_dwordx4 v[10:13], v185, s[34:35]
	s_addc_u32 s69, s65, 0
	global_load_dwordx4 v[14:17], v183, s[68:69]
	s_waitcnt lgkmcnt(8)
	s_barrier
	s_waitcnt lgkmcnt(0)
	s_setprio 1
	s_waitcnt lgkmcnt(0)
	v_mfma_f32_16x16x32_f16 v[138:141], v[146:149], v[194:197], v[138:141]
	v_mfma_f32_16x16x32_f16 v[142:145], v[154:157], v[194:197], v[142:145]
	v_mfma_f32_16x16x32_f16 v[126:129], v[146:149], v[202:205], v[126:129]
	v_mfma_f32_16x16x32_f16 v[122:125], v[154:157], v[202:205], v[122:125]
	v_mfma_f32_16x16x32_f16 v[110:113], v[146:149], v[210:213], v[110:113]
	v_mfma_f32_16x16x32_f16 v[106:109], v[154:157], v[210:213], v[106:109]
	v_mfma_f32_16x16x32_f16 v[94:97], v[146:149], v[218:221], v[94:97]
	v_mfma_f32_16x16x32_f16 v[90:93], v[154:157], v[218:221], v[90:93]
	v_mfma_f32_16x16x32_f16 v[138:141], v[150:153], v[198:201], v[138:141]
	v_mfma_f32_16x16x32_f16 v[142:145], v[158:161], v[198:201], v[142:145]
	v_mfma_f32_16x16x32_f16 v[126:129], v[150:153], v[206:209], v[126:129]
	v_mfma_f32_16x16x32_f16 v[122:125], v[158:161], v[206:209], v[122:125]
	v_mfma_f32_16x16x32_f16 v[110:113], v[150:153], v[214:217], v[110:113]
	v_mfma_f32_16x16x32_f16 v[106:109], v[158:161], v[214:217], v[106:109]
	v_mfma_f32_16x16x32_f16 v[94:97], v[150:153], v[222:225], v[94:97]
	v_mfma_f32_16x16x32_f16 v[90:93], v[158:161], v[222:225], v[90:93]
	s_setprio 0
	s_waitcnt lgkmcnt(0)
	s_setprio 1
	s_waitcnt lgkmcnt(0)
	v_mfma_f32_16x16x32_f16 v[134:137], v[226:229], v[194:197], v[134:137]
	v_mfma_f32_16x16x32_f16 v[130:133], v[234:237], v[194:197], v[130:133]
	v_mfma_f32_16x16x32_f16 v[118:121], v[226:229], v[202:205], v[118:121]
	v_mfma_f32_16x16x32_f16 v[114:117], v[234:237], v[202:205], v[114:117]
	v_mfma_f32_16x16x32_f16 v[102:105], v[226:229], v[210:213], v[102:105]
	v_mfma_f32_16x16x32_f16 v[98:101], v[234:237], v[210:213], v[98:101]
	v_mfma_f32_16x16x32_f16 v[86:89], v[226:229], v[218:221], v[86:89]
	v_mfma_f32_16x16x32_f16 v[82:85], v[234:237], v[218:221], v[82:85]
	v_mfma_f32_16x16x32_f16 v[134:137], v[230:233], v[198:201], v[134:137]
	v_mfma_f32_16x16x32_f16 v[130:133], v[238:241], v[198:201], v[130:133]
	v_mfma_f32_16x16x32_f16 v[118:121], v[230:233], v[206:209], v[118:121]
	v_mfma_f32_16x16x32_f16 v[114:117], v[238:241], v[206:209], v[114:117]
	v_mfma_f32_16x16x32_f16 v[102:105], v[230:233], v[214:217], v[102:105]
	v_mfma_f32_16x16x32_f16 v[98:101], v[238:241], v[214:217], v[98:101]
	v_mfma_f32_16x16x32_f16 v[86:89], v[230:233], v[222:225], v[86:89]
	v_mfma_f32_16x16x32_f16 v[82:85], v[238:241], v[222:225], v[82:85]
	s_setprio 0
	s_barrier
	s_add_i32 s81, s55, s45
	v_lshl_add_u64 v[170:171], v[170:171], 0, s[26:27]
	s_mov_b32 m0, s81
	global_load_lds_dwordx4 v[170:171], off
	v_lshl_add_u64 v[170:171], v[242:243], 0, s[26:27]
	s_add_i32 m0, s81, 0x2000
	s_nop 0
	global_load_lds_dwordx4 v[170:171], off
	ds_read_b128 v[194:197], v189 offset:49152
	ds_read_b128 v[198:201], v189 offset:50176
	ds_read_b128 v[202:205], v189 offset:51200
	ds_read_b128 v[206:209], v189 offset:52224
	ds_read_b128 v[210:213], v189 offset:53248
	ds_read_b128 v[214:217], v189 offset:54272
	ds_read_b128 v[218:221], v189 offset:55296
	ds_read_b128 v[222:225], v189 offset:56320
	s_add_i32 s34, s64, s70
	s_ashr_i32 s35, s34, 31
	s_waitcnt vmcnt(2)
	s_lshl_b64 s[34:35], s[34:35], 1
	v_pk_add_f16 v6, v6, v14
	v_pk_add_f16 v7, v7, v15
	v_pk_add_f16 v8, v8, v16
	v_pk_add_f16 v9, v9, v17
	s_add_u32 s34, s8, s34
	v_pk_max_f16 v9, v9, 0
	v_pk_max_f16 v8, v8, 0
	v_pk_max_f16 v7, v7, 0
	v_pk_max_f16 v6, v6, 0
	v_pk_add_f16 v10, v10, v14
	v_pk_add_f16 v11, v11, v15
	v_pk_add_f16 v12, v12, v16
	v_pk_add_f16 v13, v13, v17
	s_addc_u32 s35, s9, s35
	s_add_i32 s64, s67, s70
	v_pk_max_f16 v13, v13, 0
	v_pk_max_f16 v12, v12, 0
	v_pk_max_f16 v11, v11, 0
	v_pk_max_f16 v10, v10, 0
	ds_write_b128 v186, v[6:9] offset:32768
	ds_write_b128 v186, v[10:13] offset:40960
	s_ashr_i32 s65, s64, 31
	s_lshl_b64 s[64:65], s[64:65], 1
	s_nop 4
	global_load_dwordx4 v[14:17], v184, s[34:35]
	s_add_u32 s64, s10, s64
	global_load_dwordx4 v[6:9], v185, s[34:35]
	s_addc_u32 s65, s11, s65
	global_load_dwordx4 v[10:13], v183, s[64:65]
	s_barrier
	s_waitcnt lgkmcnt(0)
	s_setprio 1
	s_waitcnt lgkmcnt(0)
	v_mfma_f32_16x16x32_f16 v[78:81], v[146:149], v[194:197], v[78:81]
	v_mfma_f32_16x16x32_f16 v[74:77], v[154:157], v[194:197], v[74:77]
	v_mfma_f32_16x16x32_f16 v[62:65], v[146:149], v[202:205], v[62:65]
	v_mfma_f32_16x16x32_f16 v[58:61], v[154:157], v[202:205], v[58:61]
	v_mfma_f32_16x16x32_f16 v[46:49], v[146:149], v[210:213], v[46:49]
	v_mfma_f32_16x16x32_f16 v[42:45], v[154:157], v[210:213], v[42:45]
	v_mfma_f32_16x16x32_f16 v[30:33], v[146:149], v[218:221], v[30:33]
	v_mfma_f32_16x16x32_f16 v[26:29], v[154:157], v[218:221], v[26:29]
	v_mfma_f32_16x16x32_f16 v[78:81], v[150:153], v[198:201], v[78:81]
	v_mfma_f32_16x16x32_f16 v[74:77], v[158:161], v[198:201], v[74:77]
	v_mfma_f32_16x16x32_f16 v[62:65], v[150:153], v[206:209], v[62:65]
	v_mfma_f32_16x16x32_f16 v[58:61], v[158:161], v[206:209], v[58:61]
	v_mfma_f32_16x16x32_f16 v[46:49], v[150:153], v[214:217], v[46:49]
	v_mfma_f32_16x16x32_f16 v[42:45], v[158:161], v[214:217], v[42:45]
	v_mfma_f32_16x16x32_f16 v[30:33], v[150:153], v[222:225], v[30:33]
	v_mfma_f32_16x16x32_f16 v[26:29], v[158:161], v[222:225], v[26:29]
	s_setprio 0
	s_barrier
	s_add_i32 s34, s56, s45
	v_lshl_add_u64 v[146:147], v[244:245], 0, s[26:27]
	s_mov_b32 m0, s34
	s_nop 0
	global_load_lds_dwordx4 v[146:147], off
	v_lshl_add_u64 v[146:147], v[246:247], 0, s[26:27]
	s_add_i32 m0, s34, 0x2000
	s_nop 0
	global_load_lds_dwordx4 v[146:147], off
	s_waitcnt vmcnt(6)
	s_barrier
	s_setprio 1
	v_mfma_f32_16x16x32_f16 v[70:73], v[226:229], v[194:197], v[70:73]
	v_mfma_f32_16x16x32_f16 v[66:69], v[234:237], v[194:197], v[66:69]
	v_mfma_f32_16x16x32_f16 v[54:57], v[226:229], v[202:205], v[54:57]
	v_mfma_f32_16x16x32_f16 v[50:53], v[234:237], v[202:205], v[50:53]
	v_mfma_f32_16x16x32_f16 v[38:41], v[226:229], v[210:213], v[38:41]
	v_mfma_f32_16x16x32_f16 v[34:37], v[234:237], v[210:213], v[34:37]
	v_mfma_f32_16x16x32_f16 v[22:25], v[226:229], v[218:221], v[22:25]
	v_mfma_f32_16x16x32_f16 v[18:21], v[234:237], v[218:221], v[18:21]
	v_mfma_f32_16x16x32_f16 v[70:73], v[230:233], v[198:201], v[70:73]
	v_mfma_f32_16x16x32_f16 v[66:69], v[238:241], v[198:201], v[66:69]
	v_mfma_f32_16x16x32_f16 v[54:57], v[230:233], v[206:209], v[54:57]
	v_mfma_f32_16x16x32_f16 v[50:53], v[238:241], v[206:209], v[50:53]
	v_mfma_f32_16x16x32_f16 v[38:41], v[230:233], v[214:217], v[38:41]
	v_mfma_f32_16x16x32_f16 v[34:37], v[238:241], v[214:217], v[34:37]
	v_mfma_f32_16x16x32_f16 v[22:25], v[230:233], v[222:225], v[22:25]
	v_mfma_f32_16x16x32_f16 v[18:21], v[238:241], v[222:225], v[18:21]
	s_setprio 0
	s_addk_i32 s62, 0x80
	s_add_u32 s59, s59, 0x100
	s_addc_u32 s60, s60, 0
	s_cmp_ge_i32 s61, s49
	s_barrier
	s_cbranch_scc0 .LBB8_12
	s_branch .LBB8_20

.LBB8_37:
	ds_read_b128 v[144:147], v173
	ds_read_b128 v[148:151], v173 offset:1024
	ds_read_b128 v[152:155], v173 offset:2048
	ds_read_b128 v[156:159], v173 offset:3072
	ds_read_b128 v[212:215], v177
	ds_read_b128 v[216:219], v177 offset:1024
	ds_read_b128 v[220:223], v177 offset:2048
	ds_read_b128 v[224:227], v177 offset:3072
	s_cmp_eq_u32 s49, s61
	s_cselect_b64 s[24:25], -1, 0
	s_and_b64 s[24:25], s[24:25], exec
	s_cselect_b32 s35, s23, s60
	s_cselect_b32 s34, s22, s59
	s_cselect_b32 s30, 0, s61
	s_cselect_b32 s31, s56, s57
	s_lshl_b32 s24, s30, 6
	s_lshl_b32 s62, s31, 14
	s_and_b32 s68, s24, 0x180
	s_or_b32 s24, s68, s62
	s_ashr_i32 s25, s24, 31
	s_lshl_b64 s[26:27], s[24:25], 1
	s_add_u32 s28, s8, s26
	s_addc_u32 s29, s9, s27
	s_lshl_b32 s25, s31, 6
	s_lshr_b32 s26, s30, 3
	ds_read_b128 v[180:183], v174
	ds_read_b128 v[184:187], v174 offset:1024
	ds_read_b128 v[188:191], v174 offset:2048
	ds_read_b128 v[192:195], v174 offset:3072
	ds_read_b128 v[196:199], v174 offset:4096
	ds_read_b128 v[200:203], v174 offset:5120
	ds_read_b128 v[204:207], v174 offset:6144
	ds_read_b128 v[208:211], v174 offset:7168
	s_waitcnt vmcnt(2)
	s_add_i32 s25, s25, s26
	v_pk_add_f16 v8, v8, v12
	v_pk_add_f16 v9, v9, v13
	v_pk_add_f16 v10, v10, v14
	v_pk_add_f16 v11, v11, v15
	s_lshl_b32 s63, s25, 9
	v_pk_max_f16 v11, v11, 0
	v_pk_max_f16 v10, v10, 0
	v_pk_max_f16 v9, v9, 0
	v_pk_max_f16 v8, v8, 0
	v_pk_add_f16 v0, v0, v4
	v_pk_add_f16 v1, v1, v5
	v_pk_add_f16 v2, v2, v6
	v_pk_add_f16 v3, v3, v7
	s_or_b32 s26, s63, s68
	v_pk_max_f16 v3, v3, 0
	v_pk_max_f16 v2, v2, 0
	v_pk_max_f16 v1, v1, 0
	v_pk_max_f16 v0, v0, 0
	ds_write_b128 v175, v[8:11] offset:49152
	ds_write_b128 v175, v[0:3] offset:57344
	s_ashr_i32 s27, s26, 31
	s_lshl_b64 s[30:31], s[26:27], 1
	s_nop 4
	global_load_dwordx4 v[0:3], v168, s[28:29]
	s_add_u32 s30, s10, s30
	global_load_dwordx4 v[4:7], v170, s[28:29]
	s_addc_u32 s31, s11, s31
	global_load_dwordx4 v[8:11], v169, s[30:31]
	global_load_dwordx4 v[12:15], v171, s[30:31]
	s_waitcnt lgkmcnt(8)
	s_barrier
	s_waitcnt lgkmcnt(0)
	s_setprio 1
	s_waitcnt lgkmcnt(0)
	v_mfma_f32_16x16x32_f16 v[136:139], v[144:147], v[180:183], v[136:139]
	v_mfma_f32_16x16x32_f16 v[140:143], v[152:155], v[180:183], v[140:143]
	v_mfma_f32_16x16x32_f16 v[124:127], v[144:147], v[188:191], v[124:127]
	v_mfma_f32_16x16x32_f16 v[120:123], v[152:155], v[188:191], v[120:123]
	v_mfma_f32_16x16x32_f16 v[108:111], v[144:147], v[196:199], v[108:111]
	v_mfma_f32_16x16x32_f16 v[104:107], v[152:155], v[196:199], v[104:107]
	v_mfma_f32_16x16x32_f16 v[92:95], v[144:147], v[204:207], v[92:95]
	v_mfma_f32_16x16x32_f16 v[88:91], v[152:155], v[204:207], v[88:91]
	v_mfma_f32_16x16x32_f16 v[136:139], v[148:151], v[184:187], v[136:139]
	v_mfma_f32_16x16x32_f16 v[140:143], v[156:159], v[184:187], v[140:143]
	v_mfma_f32_16x16x32_f16 v[124:127], v[148:151], v[192:195], v[124:127]
	v_mfma_f32_16x16x32_f16 v[120:123], v[156:159], v[192:195], v[120:123]
	v_mfma_f32_16x16x32_f16 v[108:111], v[148:151], v[200:203], v[108:111]
	v_mfma_f32_16x16x32_f16 v[104:107], v[156:159], v[200:203], v[104:107]
	v_mfma_f32_16x16x32_f16 v[92:95], v[148:151], v[208:211], v[92:95]
	v_mfma_f32_16x16x32_f16 v[88:91], v[156:159], v[208:211], v[88:91]
	s_setprio 0
	s_waitcnt lgkmcnt(0)
	s_setprio 1
	s_waitcnt lgkmcnt(0)
	v_mfma_f32_16x16x32_f16 v[132:135], v[212:215], v[180:183], v[132:135]
	v_mfma_f32_16x16x32_f16 v[128:131], v[220:223], v[180:183], v[128:131]
	v_mfma_f32_16x16x32_f16 v[116:119], v[212:215], v[188:191], v[116:119]
	v_mfma_f32_16x16x32_f16 v[112:115], v[220:223], v[188:191], v[112:115]
	v_mfma_f32_16x16x32_f16 v[100:103], v[212:215], v[196:199], v[100:103]
	v_mfma_f32_16x16x32_f16 v[96:99], v[220:223], v[196:199], v[96:99]
	v_mfma_f32_16x16x32_f16 v[84:87], v[212:215], v[204:207], v[84:87]
	v_mfma_f32_16x16x32_f16 v[80:83], v[220:223], v[204:207], v[80:83]
	v_mfma_f32_16x16x32_f16 v[132:135], v[216:219], v[184:187], v[132:135]
	v_mfma_f32_16x16x32_f16 v[128:131], v[224:227], v[184:187], v[128:131]
	v_mfma_f32_16x16x32_f16 v[116:119], v[216:219], v[192:195], v[116:119]
	v_mfma_f32_16x16x32_f16 v[112:115], v[224:227], v[192:195], v[112:115]
	v_mfma_f32_16x16x32_f16 v[100:103], v[216:219], v[200:203], v[100:103]
	v_mfma_f32_16x16x32_f16 v[96:99], v[224:227], v[200:203], v[96:99]
	v_mfma_f32_16x16x32_f16 v[84:87], v[216:219], v[208:211], v[84:87]
	v_mfma_f32_16x16x32_f16 v[80:83], v[224:227], v[208:211], v[80:83]
	s_setprio 0
	s_or_b32 s64, s62, 0x2000
	s_or_b32 s28, s68, s64
	s_ashr_i32 s29, s28, 31
	s_barrier
	s_add_i32 s81, s51, s44
	v_lshl_add_u64 v[166:167], s[34:35], 0, v[160:161]
	s_mov_b32 m0, s81
	global_load_lds_dwordx4 v[166:167], off
	v_lshl_add_u64 v[228:229], s[34:35], 0, v[162:163]
	s_add_i32 m0, s81, 0x2000
	s_nop 0
	global_load_lds_dwordx4 v[228:229], off
	ds_read_b128 v[180:183], v174 offset:16384
	ds_read_b128 v[184:187], v174 offset:17408
	ds_read_b128 v[188:191], v174 offset:18432
	ds_read_b128 v[192:195], v174 offset:19456
	ds_read_b128 v[196:199], v174 offset:20480
	ds_read_b128 v[200:203], v174 offset:21504
	ds_read_b128 v[204:207], v174 offset:22528
	ds_read_b128 v[208:211], v174 offset:23552
	s_lshl_b64 s[30:31], s[28:29], 1
	s_waitcnt vmcnt(2)
	s_add_u32 s66, s8, s30
	v_pk_add_f16 v0, v0, v8
	v_pk_add_f16 v1, v1, v9
	v_pk_add_f16 v2, v2, v10
	v_pk_add_f16 v3, v3, v11
	s_addc_u32 s67, s9, s31
	s_add_i32 s65, s63, 0x4000
	v_pk_max_f16 v3, v3, 0
	v_pk_max_f16 v2, v2, 0
	v_pk_max_f16 v1, v1, 0
	v_pk_max_f16 v0, v0, 0
	v_pk_add_f16 v4, v4, v12
	v_pk_add_f16 v5, v5, v13
	v_pk_add_f16 v6, v6, v14
	v_pk_add_f16 v7, v7, v15
	s_or_b32 s30, s65, s68
	v_pk_max_f16 v7, v7, 0
	v_pk_max_f16 v6, v6, 0
	v_pk_max_f16 v5, v5, 0
	v_pk_max_f16 v4, v4, 0
	ds_write_b128 v175, v[0:3]
	ds_write_b128 v175, v[4:7] offset:8192
	s_ashr_i32 s31, s30, 31
	s_lshl_b64 s[68:69], s[30:31], 1
	s_nop 4
	global_load_dwordx4 v[0:3], v168, s[66:67]
	s_add_u32 s68, s10, s68
	global_load_dwordx4 v[4:7], v170, s[66:67]
	s_addc_u32 s69, s11, s69
	global_load_dwordx4 v[8:11], v169, s[68:69]
	global_load_dwordx4 v[12:15], v171, s[68:69]
	s_barrier
	s_waitcnt lgkmcnt(0)
	s_setprio 1
	s_waitcnt lgkmcnt(0)
	v_mfma_f32_16x16x32_f16 v[76:79], v[144:147], v[180:183], v[76:79]
	v_mfma_f32_16x16x32_f16 v[72:75], v[152:155], v[180:183], v[72:75]
	v_mfma_f32_16x16x32_f16 v[60:63], v[144:147], v[188:191], v[60:63]
	v_mfma_f32_16x16x32_f16 v[56:59], v[152:155], v[188:191], v[56:59]
	v_mfma_f32_16x16x32_f16 v[44:47], v[144:147], v[196:199], v[44:47]
	v_mfma_f32_16x16x32_f16 v[40:43], v[152:155], v[196:199], v[40:43]
	v_mfma_f32_16x16x32_f16 v[28:31], v[144:147], v[204:207], v[28:31]
	v_mfma_f32_16x16x32_f16 v[24:27], v[152:155], v[204:207], v[24:27]
	v_mfma_f32_16x16x32_f16 v[76:79], v[148:151], v[184:187], v[76:79]
	v_mfma_f32_16x16x32_f16 v[72:75], v[156:159], v[184:187], v[72:75]
	v_mfma_f32_16x16x32_f16 v[60:63], v[148:151], v[192:195], v[60:63]
	v_mfma_f32_16x16x32_f16 v[56:59], v[156:159], v[192:195], v[56:59]
	v_mfma_f32_16x16x32_f16 v[44:47], v[148:151], v[200:203], v[44:47]
	v_mfma_f32_16x16x32_f16 v[40:43], v[156:159], v[200:203], v[40:43]
	v_mfma_f32_16x16x32_f16 v[28:31], v[148:151], v[208:211], v[28:31]
	v_mfma_f32_16x16x32_f16 v[24:27], v[156:159], v[208:211], v[24:27]
	s_setprio 0
	s_barrier
	s_add_u32 s34, s34, s14
	s_addc_u32 s35, s35, s15
	s_add_i32 s25, s52, s44
	v_lshl_add_u64 v[230:231], s[34:35], 0, v[160:161]
	s_mov_b32 m0, s25
	v_lshl_add_u64 v[232:233], s[34:35], 0, v[162:163]
	global_load_lds_dwordx4 v[230:231], off
	s_add_i32 m0, s25, 0x2000
	s_nop 0
	global_load_lds_dwordx4 v[232:233], off
	s_waitcnt vmcnt(6)
	s_barrier
	s_setprio 1
	v_mfma_f32_16x16x32_f16 v[68:71], v[212:215], v[180:183], v[68:71]
	v_mfma_f32_16x16x32_f16 v[64:67], v[220:223], v[180:183], v[64:67]
	v_mfma_f32_16x16x32_f16 v[52:55], v[212:215], v[188:191], v[52:55]
	v_mfma_f32_16x16x32_f16 v[48:51], v[220:223], v[188:191], v[48:51]
	v_mfma_f32_16x16x32_f16 v[36:39], v[212:215], v[196:199], v[36:39]
	v_mfma_f32_16x16x32_f16 v[32:35], v[220:223], v[196:199], v[32:35]
	v_mfma_f32_16x16x32_f16 v[20:23], v[212:215], v[204:207], v[20:23]
	v_mfma_f32_16x16x32_f16 v[16:19], v[220:223], v[204:207], v[16:19]
	v_mfma_f32_16x16x32_f16 v[68:71], v[216:219], v[184:187], v[68:71]
	v_mfma_f32_16x16x32_f16 v[64:67], v[224:227], v[184:187], v[64:67]
	v_mfma_f32_16x16x32_f16 v[52:55], v[216:219], v[192:195], v[52:55]
	v_mfma_f32_16x16x32_f16 v[48:51], v[224:227], v[192:195], v[48:51]
	v_mfma_f32_16x16x32_f16 v[36:39], v[216:219], v[200:203], v[36:39]
	v_mfma_f32_16x16x32_f16 v[32:35], v[224:227], v[200:203], v[32:35]
	v_mfma_f32_16x16x32_f16 v[20:23], v[216:219], v[208:211], v[20:23]
	v_mfma_f32_16x16x32_f16 v[16:19], v[224:227], v[208:211], v[16:19]
	s_setprio 0
	s_barrier
	ds_read_b128 v[144:147], v178
	ds_read_b128 v[148:151], v178 offset:1024
	ds_read_b128 v[152:155], v178 offset:2048
	ds_read_b128 v[156:159], v178 offset:3072
	ds_read_b128 v[212:215], v179
	ds_read_b128 v[216:219], v179 offset:1024
	ds_read_b128 v[220:223], v179 offset:2048
	ds_read_b128 v[224:227], v179 offset:3072
	s_ashr_i32 s25, s62, 31
	s_lshl_b64 s[24:25], s[24:25], 1
	s_add_u32 s24, s8, s24
	s_addc_u32 s25, s9, s25
	ds_read_b128 v[180:183], v174 offset:32768
	ds_read_b128 v[184:187], v174 offset:33792
	ds_read_b128 v[188:191], v174 offset:34816
	ds_read_b128 v[192:195], v174 offset:35840
	ds_read_b128 v[196:199], v174 offset:36864
	ds_read_b128 v[200:203], v174 offset:37888
	ds_read_b128 v[204:207], v174 offset:38912
	ds_read_b128 v[208:211], v174 offset:39936
	s_waitcnt vmcnt(2)
	s_add_u32 s24, s24, 0x80
	v_pk_add_f16 v0, v0, v8
	v_pk_add_f16 v1, v1, v9
	v_pk_add_f16 v2, v2, v10
	v_pk_add_f16 v3, v3, v11
	s_addc_u32 s25, s25, 0
	s_ashr_i32 s27, s63, 31
	v_pk_max_f16 v3, v3, 0
	v_pk_max_f16 v2, v2, 0
	v_pk_max_f16 v1, v1, 0
	v_pk_max_f16 v0, v0, 0
	v_pk_add_f16 v4, v4, v12
	v_pk_add_f16 v5, v5, v13
	v_pk_add_f16 v6, v6, v14
	v_pk_add_f16 v7, v7, v15
	s_lshl_b64 s[26:27], s[26:27], 1
	v_pk_max_f16 v7, v7, 0
	v_pk_max_f16 v6, v6, 0
	v_pk_max_f16 v5, v5, 0
	v_pk_max_f16 v4, v4, 0
	ds_write_b128 v175, v[0:3] offset:16384
	ds_write_b128 v175, v[4:7] offset:24576
	s_add_u32 s26, s10, s26
	s_addc_u32 s27, s11, s27
	s_nop 4
	global_load_dwordx4 v[0:3], v168, s[24:25]
	s_add_u32 s26, s26, 0x80
	global_load_dwordx4 v[4:7], v170, s[24:25]
	s_addc_u32 s27, s27, 0
	global_load_dwordx4 v[8:11], v169, s[26:27]
	global_load_dwordx4 v[12:15], v171, s[26:27]
	s_waitcnt lgkmcnt(8)
	s_barrier
	s_waitcnt lgkmcnt(0)
	s_setprio 1
	s_waitcnt lgkmcnt(0)
	v_mfma_f32_16x16x32_f16 v[136:139], v[144:147], v[180:183], v[136:139]
	v_mfma_f32_16x16x32_f16 v[140:143], v[152:155], v[180:183], v[140:143]
	v_mfma_f32_16x16x32_f16 v[124:127], v[144:147], v[188:191], v[124:127]
	v_mfma_f32_16x16x32_f16 v[120:123], v[152:155], v[188:191], v[120:123]
	v_mfma_f32_16x16x32_f16 v[108:111], v[144:147], v[196:199], v[108:111]
	v_mfma_f32_16x16x32_f16 v[104:107], v[152:155], v[196:199], v[104:107]
	v_mfma_f32_16x16x32_f16 v[92:95], v[144:147], v[204:207], v[92:95]
	v_mfma_f32_16x16x32_f16 v[88:91], v[152:155], v[204:207], v[88:91]
	v_mfma_f32_16x16x32_f16 v[136:139], v[148:151], v[184:187], v[136:139]
	v_mfma_f32_16x16x32_f16 v[140:143], v[156:159], v[184:187], v[140:143]
	v_mfma_f32_16x16x32_f16 v[124:127], v[148:151], v[192:195], v[124:127]
	v_mfma_f32_16x16x32_f16 v[120:123], v[156:159], v[192:195], v[120:123]
	v_mfma_f32_16x16x32_f16 v[108:111], v[148:151], v[200:203], v[108:111]
	v_mfma_f32_16x16x32_f16 v[104:107], v[156:159], v[200:203], v[104:107]
	v_mfma_f32_16x16x32_f16 v[92:95], v[148:151], v[208:211], v[92:95]
	v_mfma_f32_16x16x32_f16 v[88:91], v[156:159], v[208:211], v[88:91]
	s_setprio 0
	s_waitcnt lgkmcnt(0)
	s_setprio 1
	s_waitcnt lgkmcnt(0)
	v_mfma_f32_16x16x32_f16 v[132:135], v[212:215], v[180:183], v[132:135]
	v_mfma_f32_16x16x32_f16 v[128:131], v[220:223], v[180:183], v[128:131]
	v_mfma_f32_16x16x32_f16 v[116:119], v[212:215], v[188:191], v[116:119]
	v_mfma_f32_16x16x32_f16 v[112:115], v[220:223], v[188:191], v[112:115]
	v_mfma_f32_16x16x32_f16 v[100:103], v[212:215], v[196:199], v[100:103]
	v_mfma_f32_16x16x32_f16 v[96:99], v[220:223], v[196:199], v[96:99]
	v_mfma_f32_16x16x32_f16 v[84:87], v[212:215], v[204:207], v[84:87]
	v_mfma_f32_16x16x32_f16 v[80:83], v[220:223], v[204:207], v[80:83]
	v_mfma_f32_16x16x32_f16 v[132:135], v[216:219], v[184:187], v[132:135]
	v_mfma_f32_16x16x32_f16 v[128:131], v[224:227], v[184:187], v[128:131]
	v_mfma_f32_16x16x32_f16 v[116:119], v[216:219], v[192:195], v[116:119]
	v_mfma_f32_16x16x32_f16 v[112:115], v[224:227], v[192:195], v[112:115]
	v_mfma_f32_16x16x32_f16 v[100:103], v[216:219], v[200:203], v[100:103]
	v_mfma_f32_16x16x32_f16 v[96:99], v[224:227], v[200:203], v[96:99]
	v_mfma_f32_16x16x32_f16 v[84:87], v[216:219], v[208:211], v[84:87]
	v_mfma_f32_16x16x32_f16 v[80:83], v[224:227], v[208:211], v[80:83]
	s_setprio 0
	s_ashr_i32 s29, s64, 31
	s_lshl_b64 s[24:25], s[28:29], 1
	s_add_u32 s24, s8, s24
	s_barrier
	s_add_i32 s81, s53, s44
	v_lshl_add_u64 v[166:167], v[166:167], 0, s[20:21]
	s_mov_b32 m0, s81
	global_load_lds_dwordx4 v[166:167], off
	v_lshl_add_u64 v[166:167], v[228:229], 0, s[20:21]
	s_add_i32 m0, s81, 0x2000
	s_nop 0
	global_load_lds_dwordx4 v[166:167], off
	ds_read_b128 v[180:183], v174 offset:49152
	ds_read_b128 v[184:187], v174 offset:50176
	ds_read_b128 v[188:191], v174 offset:51200
	ds_read_b128 v[192:195], v174 offset:52224
	ds_read_b128 v[196:199], v174 offset:53248
	ds_read_b128 v[200:203], v174 offset:54272
	ds_read_b128 v[204:207], v174 offset:55296
	ds_read_b128 v[208:211], v174 offset:56320
	s_addc_u32 s25, s9, s25
	s_waitcnt vmcnt(2)
	s_add_u32 s24, s24, 0x80
	v_pk_add_f16 v0, v0, v8
	v_pk_add_f16 v1, v1, v9
	v_pk_add_f16 v2, v2, v10
	v_pk_add_f16 v3, v3, v11
	s_addc_u32 s25, s25, 0
	s_ashr_i32 s31, s65, 31
	v_pk_max_f16 v3, v3, 0
	v_pk_max_f16 v2, v2, 0
	v_pk_max_f16 v1, v1, 0
	v_pk_max_f16 v0, v0, 0
	v_pk_add_f16 v4, v4, v12
	v_pk_add_f16 v5, v5, v13
	v_pk_add_f16 v6, v6, v14
	v_pk_add_f16 v7, v7, v15
	s_lshl_b64 s[26:27], s[30:31], 1
	v_pk_max_f16 v7, v7, 0
	v_pk_max_f16 v6, v6, 0
	v_pk_max_f16 v5, v5, 0
	v_pk_max_f16 v4, v4, 0
	ds_write_b128 v175, v[0:3] offset:32768
	ds_write_b128 v175, v[4:7] offset:40960
	s_add_u32 s26, s10, s26
	s_addc_u32 s27, s11, s27
	s_nop 4
	global_load_dwordx4 v[8:11], v168, s[24:25]
	s_add_u32 s26, s26, 0x80
	global_load_dwordx4 v[0:3], v170, s[24:25]
	s_addc_u32 s27, s27, 0
	global_load_dwordx4 v[12:15], v169, s[26:27]
	global_load_dwordx4 v[4:7], v171, s[26:27]
	s_barrier
	s_waitcnt lgkmcnt(0)
	s_setprio 1
	s_waitcnt lgkmcnt(0)
	v_mfma_f32_16x16x32_f16 v[76:79], v[144:147], v[180:183], v[76:79]
	v_mfma_f32_16x16x32_f16 v[72:75], v[152:155], v[180:183], v[72:75]
	v_mfma_f32_16x16x32_f16 v[60:63], v[144:147], v[188:191], v[60:63]
	v_mfma_f32_16x16x32_f16 v[56:59], v[152:155], v[188:191], v[56:59]
	v_mfma_f32_16x16x32_f16 v[44:47], v[144:147], v[196:199], v[44:47]
	v_mfma_f32_16x16x32_f16 v[40:43], v[152:155], v[196:199], v[40:43]
	v_mfma_f32_16x16x32_f16 v[28:31], v[144:147], v[204:207], v[28:31]
	v_mfma_f32_16x16x32_f16 v[24:27], v[152:155], v[204:207], v[24:27]
	v_mfma_f32_16x16x32_f16 v[76:79], v[148:151], v[184:187], v[76:79]
	v_mfma_f32_16x16x32_f16 v[72:75], v[156:159], v[184:187], v[72:75]
	v_mfma_f32_16x16x32_f16 v[60:63], v[148:151], v[192:195], v[60:63]
	v_mfma_f32_16x16x32_f16 v[56:59], v[156:159], v[192:195], v[56:59]
	v_mfma_f32_16x16x32_f16 v[44:47], v[148:151], v[200:203], v[44:47]
	v_mfma_f32_16x16x32_f16 v[40:43], v[156:159], v[200:203], v[40:43]
	v_mfma_f32_16x16x32_f16 v[28:31], v[148:151], v[208:211], v[28:31]
	v_mfma_f32_16x16x32_f16 v[24:27], v[156:159], v[208:211], v[24:27]
	s_setprio 0
	s_barrier
	s_add_i32 s24, s54, s44
	v_lshl_add_u64 v[144:145], v[230:231], 0, s[20:21]
	s_mov_b32 m0, s24
	s_nop 0
	global_load_lds_dwordx4 v[144:145], off
	v_lshl_add_u64 v[144:145], v[232:233], 0, s[20:21]
	s_add_i32 m0, s24, 0x2000
	s_nop 0
	global_load_lds_dwordx4 v[144:145], off
	s_waitcnt vmcnt(6)
	s_barrier
	s_setprio 1
	v_mfma_f32_16x16x32_f16 v[68:71], v[212:215], v[180:183], v[68:71]
	v_mfma_f32_16x16x32_f16 v[64:67], v[220:223], v[180:183], v[64:67]
	v_mfma_f32_16x16x32_f16 v[52:55], v[212:215], v[188:191], v[52:55]
	v_mfma_f32_16x16x32_f16 v[48:51], v[220:223], v[188:191], v[48:51]
	v_mfma_f32_16x16x32_f16 v[36:39], v[212:215], v[196:199], v[36:39]
	v_mfma_f32_16x16x32_f16 v[32:35], v[220:223], v[196:199], v[32:35]
	v_mfma_f32_16x16x32_f16 v[20:23], v[212:215], v[204:207], v[20:23]
	v_mfma_f32_16x16x32_f16 v[16:19], v[220:223], v[204:207], v[16:19]
	v_mfma_f32_16x16x32_f16 v[68:71], v[216:219], v[184:187], v[68:71]
	v_mfma_f32_16x16x32_f16 v[64:67], v[224:227], v[184:187], v[64:67]
	v_mfma_f32_16x16x32_f16 v[52:55], v[216:219], v[192:195], v[52:55]
	v_mfma_f32_16x16x32_f16 v[48:51], v[224:227], v[192:195], v[48:51]
	v_mfma_f32_16x16x32_f16 v[36:39], v[216:219], v[200:203], v[36:39]
	v_mfma_f32_16x16x32_f16 v[32:35], v[224:227], v[200:203], v[32:35]
	v_mfma_f32_16x16x32_f16 v[20:23], v[216:219], v[208:211], v[20:23]
	v_mfma_f32_16x16x32_f16 v[16:19], v[224:227], v[208:211], v[16:19]
	s_setprio 0
	s_add_i32 s24, s61, 2
	s_add_u32 s59, s59, 0x100
	s_addc_u32 s60, s60, 0
	s_cmp_ge_i32 s61, s49
	s_mov_b32 s61, s24
	s_barrier
	s_cbranch_scc0 .LBB8_37
	s_branch .LBB8_45

	.amdhsa_kernel _Z14k_phase_gen_utIN3pg86EpiH16ILb0ELb1EEENS1_ILb1ELb0EEEEvNS0_4GemmES4_NS0_6GenSrcET_T0_
		.amdhsa_group_segment_fixed_size 0
		.amdhsa_private_segment_fixed_size 0
		.amdhsa_kernarg_size 384
		.amdhsa_user_sgpr_count 2
		.amdhsa_user_sgpr_dispatch_ptr 0
		.amdhsa_user_sgpr_queue_ptr 0
		.amdhsa_user_sgpr_kernarg_segment_ptr 1
		.amdhsa_user_sgpr_dispatch_id 0
		.amdhsa_user_sgpr_kernarg_preload_length 0
		.amdhsa_user_sgpr_kernarg_preload_offset 0
		.amdhsa_user_sgpr_private_segment_size 0
		.amdhsa_uses_dynamic_stack 0
		.amdhsa_enable_private_segment 0
		.amdhsa_system_sgpr_workgroup_id_x 1
		.amdhsa_system_sgpr_workgroup_id_y 0
		.amdhsa_system_sgpr_workgroup_id_z 0
		.amdhsa_system_sgpr_workgroup_info 0
		.amdhsa_system_vgpr_workitem_id 0
		.amdhsa_next_free_vgpr 248
		.amdhsa_next_free_sgpr 82
		.amdhsa_accum_offset 248
		.amdhsa_reserve_vcc 1
		.amdhsa_float_round_mode_32 0
		.amdhsa_float_round_mode_16_64 0
		.amdhsa_float_denorm_mode_32 3
		.amdhsa_float_denorm_mode_16_64 3
		.amdhsa_dx10_clamp 1
		.amdhsa_ieee_mode 1
		.amdhsa_fp16_overflow 0
		.amdhsa_tg_split 0
		.amdhsa_exception_fp_ieee_invalid_op 0
		.amdhsa_exception_fp_denorm_src 0
		.amdhsa_exception_fp_ieee_div_zero 0
		.amdhsa_exception_fp_ieee_overflow 0
		.amdhsa_exception_fp_ieee_underflow 0
		.amdhsa_exception_fp_ieee_inexact 0
		.amdhsa_exception_int_div_zero 0
	.end_amdhsa_kernel

amdhsa.kernels:
  - .agpr_count:     0
    .args:
      - .offset:         0
        .size:           32
        .value_kind:     by_value
      - .address_space:  global
        .offset:         32
        .size:           8
        .value_kind:     global_buffer
      - .address_space:  global
        .offset:         40
        .size:           8
        .value_kind:     global_buffer
      - .offset:         48
        .size:           4
        .value_kind:     by_value
      - .offset:         56
        .size:           4
        .value_kind:     hidden_block_count_x
      - .offset:         60
        .size:           4
        .value_kind:     hidden_block_count_y
      - .offset:         64
        .size:           4
        .value_kind:     hidden_block_count_z
      - .offset:         68
        .size:           2
        .value_kind:     hidden_group_size_x
      - .offset:         70
        .size:           2
        .value_kind:     hidden_group_size_y
      - .offset:         72
        .size:           2
        .value_kind:     hidden_group_size_z
      - .offset:         74
        .size:           2
        .value_kind:     hidden_remainder_x
      - .offset:         76
        .size:           2
        .value_kind:     hidden_remainder_y
      - .offset:         78
        .size:           2
        .value_kind:     hidden_remainder_z
      - .offset:         96
        .size:           8
        .value_kind:     hidden_global_offset_x
      - .offset:         104
        .size:           8
        .value_kind:     hidden_global_offset_y
      - .offset:         112
        .size:           8
        .value_kind:     hidden_global_offset_z
      - .offset:         120
        .size:           2
        .value_kind:     hidden_grid_dims
      - .offset:         176
        .size:           4
        .value_kind:     hidden_dynamic_lds_size
    .group_segment_fixed_size: 0
    .kernarg_segment_align: 8
    .kernarg_segment_size: 312
    .language:       OpenCL C
    .language_version:
      - 2
      - 0
    .max_flat_workgroup_size: 512
    .name:           _Z10k_phase_hmN3pg84GemmEPDF16_PKfi
    .private_segment_fixed_size: 0
    .sgpr_count:     68
    .sgpr_spill_count: 0
    .symbol:         _Z10k_phase_hmN3pg84GemmEPDF16_PKfi.kd
    .uniform_work_group_size: 1
    .uses_dynamic_stack: false
    .vgpr_count:     140
    .vgpr_spill_count: 0
    .wavefront_size: 64
  - .agpr_count:     0
    .args:
      - .offset:         0
        .size:           32
        .value_kind:     by_value
      - .address_space:  global
        .offset:         32
        .size:           8
        .value_kind:     global_buffer
      - .address_space:  global
        .offset:         40
        .size:           8
        .value_kind:     global_buffer
      - .offset:         48
        .size:           4
        .value_kind:     by_value
      - .offset:         56
        .size:           4
        .value_kind:     hidden_block_count_x
      - .offset:         60
        .size:           4
        .value_kind:     hidden_block_count_y
      - .offset:         64
        .size:           4
        .value_kind:     hidden_block_count_z
      - .offset:         68
        .size:           2
        .value_kind:     hidden_group_size_x
      - .offset:         70
        .size:           2
        .value_kind:     hidden_group_size_y
      - .offset:         72
        .size:           2
        .value_kind:     hidden_group_size_z
      - .offset:         74
        .size:           2
        .value_kind:     hidden_remainder_x
      - .offset:         76
        .size:           2
        .value_kind:     hidden_remainder_y
      - .offset:         78
        .size:           2
        .value_kind:     hidden_remainder_z
      - .offset:         96
        .size:           8
        .value_kind:     hidden_global_offset_x
      - .offset:         104
        .size:           8
        .value_kind:     hidden_global_offset_y
      - .offset:         112
        .size:           8
        .value_kind:     hidden_global_offset_z
      - .offset:         120
        .size:           2
        .value_kind:     hidden_grid_dims
      - .offset:         176
        .size:           4
        .value_kind:     hidden_dynamic_lds_size
    .group_segment_fixed_size: 0
    .kernarg_segment_align: 8
    .kernarg_segment_size: 312
    .language:       OpenCL C
    .language_version:
      - 2
      - 0
    .max_flat_workgroup_size: 512
    .name:           _Z10k_phase_qmN3pg84GemmEPDF16_PKfi
    .private_segment_fixed_size: 0
    .sgpr_count:     67
    .sgpr_spill_count: 0
    .symbol:         _Z10k_phase_qmN3pg84GemmEPDF16_PKfi.kd
    .uniform_work_group_size: 1
    .uses_dynamic_stack: false
    .vgpr_count:     102
    .vgpr_spill_count: 0
    .wavefront_size: 64
  - .agpr_count:     0
    .args:
      - .offset:         0
        .size:           288
        .value_kind:     by_value
    .group_segment_fixed_size: 16640
    .kernarg_segment_align: 8
    .kernarg_segment_size: 288
    .language:       OpenCL C
    .language_version:
      - 2
      - 0
    .max_flat_workgroup_size: 256
    .name:           _Z11prep_kernel8PrepArgs
    .private_segment_fixed_size: 0
    .sgpr_count:     26
    .sgpr_spill_count: 0
    .symbol:         _Z11prep_kernel8PrepArgs.kd
    .uniform_work_group_size: 1
    .uses_dynamic_stack: false
    .vgpr_count:     35
    .vgpr_spill_count: 0
    .wavefront_size: 64
  - .agpr_count:     0
    .args:
      - .actual_access:  read_only
        .address_space:  global
        .offset:         0
        .size:           8
        .value_kind:     global_buffer
      - .actual_access:  read_only
        .address_space:  global
        .offset:         8
        .size:           8
        .value_kind:     global_buffer
      - .actual_access:  read_only
        .address_space:  global
        .offset:         16
        .size:           8
        .value_kind:     global_buffer
      - .actual_access:  write_only
        .address_space:  global
        .offset:         24
        .size:           8
        .value_kind:     global_buffer
    .group_segment_fixed_size: 0
    .kernarg_segment_align: 8
    .kernarg_segment_size: 32
    .language:       OpenCL C
    .language_version:
      - 2
      - 0
    .max_flat_workgroup_size: 256
    .name:           _Z11leaf_kernelPKfS0_PKiPDF16_
    .private_segment_fixed_size: 0
    .sgpr_count:     18
    .sgpr_spill_count: 0
    .symbol:         _Z11leaf_kernelPKfS0_PKiPDF16_.kd
    .uniform_work_group_size: 1
    .uses_dynamic_stack: false
    .vgpr_count:     25
    .vgpr_spill_count: 0
    .wavefront_size: 64
  - .agpr_count:     248
    .args:
      - .actual_access:  read_only
        .address_space:  global
        .offset:         0
        .size:           8
        .value_kind:     global_buffer
      - .actual_access:  read_only
        .address_space:  global
        .offset:         8
        .size:           8
        .value_kind:     global_buffer
      - .actual_access:  write_only
        .address_space:  global
        .offset:         16
        .size:           8
        .value_kind:     global_buffer
      - .actual_access:  write_only
        .address_space:  global
        .offset:         24
        .size:           8
        .value_kind:     global_buffer
    .group_segment_fixed_size: 0
    .kernarg_segment_align: 8
    .kernarg_segment_size: 32
    .language:       OpenCL C
    .language_version:
      - 2
      - 0
    .max_flat_workgroup_size: 256
    .name:           _Z10rnn_kernelPKDF16_S0_PDF16_S1_
    .private_segment_fixed_size: 0
    .sgpr_count:     22
    .sgpr_spill_count: 0
    .symbol:         _Z10rnn_kernelPKDF16_S0_PDF16_S1_.kd
    .uniform_work_group_size: 1
    .uses_dynamic_stack: false
    .vgpr_count:     496
    .vgpr_spill_count: 0
    .wavefront_size: 64
  - .agpr_count:     0
    .args:
      - .actual_access:  read_only
        .address_space:  global
        .offset:         0
        .size:           8
        .value_kind:     global_buffer
      - .actual_access:  read_only
        .address_space:  global
        .offset:         8
        .size:           8
        .value_kind:     global_buffer
      - .actual_access:  write_only
        .address_space:  global
        .offset:         16
        .size:           8
        .value_kind:     global_buffer
    .group_segment_fixed_size: 0
    .kernarg_segment_align: 8
    .kernarg_segment_size: 24
    .language:       OpenCL C
    .language_version:
      - 2
      - 0
    .max_flat_workgroup_size: 256
    .name:           _Z10max_kernelPKDF16_S0_PDF16_
    .private_segment_fixed_size: 0
    .sgpr_count:     18
    .sgpr_spill_count: 0
    .symbol:         _Z10max_kernelPKDF16_S0_PDF16_.kd
    .uniform_work_group_size: 1
    .uses_dynamic_stack: false
    .vgpr_count:     38
    .vgpr_spill_count: 0
    .wavefront_size: 64
  - .agpr_count:     0
    .args:
      - .actual_access:  read_only
        .address_space:  global
        .offset:         0
        .size:           8
        .value_kind:     global_buffer
      - .actual_access:  read_only
        .address_space:  global
        .offset:         8
        .size:           8
        .value_kind:     global_buffer
      - .actual_access:  read_only
        .address_space:  global
        .offset:         16
        .size:           8
        .value_kind:     global_buffer
      - .actual_access:  write_only
        .address_space:  global
        .offset:         24
        .size:           8
        .value_kind:     global_buffer
    .group_segment_fixed_size: 0
    .kernarg_segment_align: 8
    .kernarg_segment_size: 32
    .language:       OpenCL C
    .language_version:
      - 2
      - 0
    .max_flat_workgroup_size: 256
    .name:           _Z12final_kernelPKfS0_S0_Pf
    .private_segment_fixed_size: 0
    .sgpr_count:     14
    .sgpr_spill_count: 0
    .symbol:         _Z12final_kernelPKfS0_S0_Pf.kd
    .uniform_work_group_size: 1
    .uses_dynamic_stack: false
    .vgpr_count:     23
    .vgpr_spill_count: 0
    .wavefront_size: 64
  - .agpr_count:     0
    .args:
      - .address_space:  global
        .offset:         0
        .size:           8
        .value_kind:     global_buffer
      - .offset:         8
        .size:           4
        .value_kind:     by_value
      - .address_space:  global
        .offset:         16
        .size:           8
        .value_kind:     global_buffer
      - .offset:         24
        .size:           4
        .value_kind:     by_value
      - .actual_access:  write_only
        .address_space:  global
        .offset:         32
        .size:           8
        .value_kind:     global_buffer
      - .offset:         40
        .size:           4
        .value_kind:     by_value
      - .actual_access:  read_only
        .address_space:  global
        .offset:         48
        .size:           8
        .value_kind:     global_buffer
    .group_segment_fixed_size: 0
    .kernarg_segment_align: 8
    .kernarg_segment_size: 56
    .language:       OpenCL C
    .language_version:
      - 2
      - 0
    .max_flat_workgroup_size: 512
    .name:           _Z9tg_kernelILi64ELi8ELi3ELb0EEvPKDF16_iS1_iPviPKf
    .private_segment_fixed_size: 0
    .sgpr_count:     26
    .sgpr_spill_count: 0
    .symbol:         _Z9tg_kernelILi64ELi8ELi3ELb0EEvPKDF16_iS1_iPviPKf.kd
    .uniform_work_group_size: 1
    .uses_dynamic_stack: false
    .vgpr_count:     62
    .vgpr_spill_count: 0
    .wavefront_size: 64
  - .agpr_count:     0
    .args:
      - .offset:         0
        .size:           32
        .value_kind:     by_value
      - .offset:         32
        .size:           32
        .value_kind:     by_value
      - .offset:         64
        .size:           16
        .value_kind:     by_value
      - .offset:         80
        .size:           24
        .value_kind:     by_value
      - .offset:         104
        .size:           24
        .value_kind:     by_value
      - .offset:         128
        .size:           4
        .value_kind:     hidden_block_count_x
      - .offset:         132
        .size:           4
        .value_kind:     hidden_block_count_y
      - .offset:         136
        .size:           4
        .value_kind:     hidden_block_count_z
      - .offset:         140
        .size:           2
        .value_kind:     hidden_group_size_x
      - .offset:         142
        .size:           2
        .value_kind:     hidden_group_size_y
      - .offset:         144
        .size:           2
        .value_kind:     hidden_group_size_z
      - .offset:         146
        .size:           2
        .value_kind:     hidden_remainder_x
      - .offset:         148
        .size:           2
        .value_kind:     hidden_remainder_y
      - .offset:         150
        .size:           2
        .value_kind:     hidden_remainder_z
      - .offset:         168
        .size:           8
        .value_kind:     hidden_global_offset_x
      - .offset:         176
        .size:           8
        .value_kind:     hidden_global_offset_y
      - .offset:         184
        .size:           8
        .value_kind:     hidden_global_offset_z
      - .offset:         192
        .size:           2
        .value_kind:     hidden_grid_dims
      - .offset:         248
        .size:           4
        .value_kind:     hidden_dynamic_lds_size
    .group_segment_fixed_size: 0
    .kernarg_segment_align: 8
    .kernarg_segment_size: 384
    .language:       OpenCL C
    .language_version:
      - 2
      - 0
    .max_flat_workgroup_size: 512
    .name:           _Z14k_phase_gen_utIN3pg86EpiH16ILb0ELb1EEENS1_ILb1ELb0EEEEvNS0_4GemmES4_NS0_6GenSrcET_T0_
    .private_segment_fixed_size: 0
    .sgpr_count:     88
    .sgpr_spill_count: 0
    .symbol:         _Z14k_phase_gen_utIN3pg86EpiH16ILb0ELb1EEENS1_ILb1ELb0EEEEvNS0_4GemmES4_NS0_6GenSrcET_T0_.kd
    .uniform_work_group_size: 1
    .uses_dynamic_stack: false
    .vgpr_count:     248
    .vgpr_spill_count: 0
    .wavefront_size: 64
  - .agpr_count:     0
    .args:
      - .address_space:  global
        .offset:         0
        .size:           8
        .value_kind:     global_buffer
      - .offset:         8
        .size:           4
        .value_kind:     by_value
      - .address_space:  global
        .offset:         16
        .size:           8
        .value_kind:     global_buffer
      - .offset:         24
        .size:           4
        .value_kind:     by_value
      - .actual_access:  write_only
        .address_space:  global
        .offset:         32
        .size:           8
        .value_kind:     global_buffer
      - .offset:         40
        .size:           4
        .value_kind:     by_value
      - .actual_access:  read_only
        .address_space:  global
        .offset:         48
        .size:           8
        .value_kind:     global_buffer
      - .offset:         56
        .size:           4
        .value_kind:     hidden_block_count_x
      - .offset:         60
        .size:           4
        .value_kind:     hidden_block_count_y
      - .offset:         64
        .size:           4
        .value_kind:     hidden_block_count_z
      - .offset:         68
        .size:           2
        .value_kind:     hidden_group_size_x
      - .offset:         70
        .size:           2
        .value_kind:     hidden_group_size_y
      - .offset:         72
        .size:           2
        .value_kind:     hidden_group_size_z
      - .offset:         74
        .size:           2
        .value_kind:     hidden_remainder_x
      - .offset:         76
        .size:           2
        .value_kind:     hidden_remainder_y
      - .offset:         78
        .size:           2
        .value_kind:     hidden_remainder_z
      - .offset:         96
        .size:           8
        .value_kind:     hidden_global_offset_x
      - .offset:         104
        .size:           8
        .value_kind:     hidden_global_offset_y
      - .offset:         112
        .size:           8
        .value_kind:     hidden_global_offset_z
      - .offset:         120
        .size:           2
        .value_kind:     hidden_grid_dims
      - .offset:         176
        .size:           4
        .value_kind:     hidden_dynamic_lds_size
    .group_segment_fixed_size: 0
    .kernarg_segment_align: 8
    .kernarg_segment_size: 312
    .language:       OpenCL C
    .language_version:
      - 2
      - 0
    .max_flat_workgroup_size: 512
    .name:           _Z9tg_kernelILi128ELi8ELi1ELb1EEvPKDF16_iS1_iPviPKf
    .private_segment_fixed_size: 0
    .sgpr_count:     25
    .sgpr_spill_count: 0
    .symbol:         _Z9tg_kernelILi128ELi8ELi1ELb1EEvPKDF16_iS1_iPviPKf.kd
    .uniform_work_group_size: 1
    .uses_dynamic_stack: false
    .vgpr_count:     96
    .vgpr_spill_count: 0
    .wavefront_size: 64
  - .agpr_count:     0
    .args:
      - .address_space:  global
        .offset:         0
        .size:           8
        .value_kind:     global_buffer
      - .offset:         8
        .size:           4
        .value_kind:     by_value
      - .address_space:  global
        .offset:         16
        .size:           8
        .value_kind:     global_buffer
      - .offset:         24
        .size:           4
        .value_kind:     by_value
      - .actual_access:  write_only
        .address_space:  global
        .offset:         32
        .size:           8
        .value_kind:     global_buffer
      - .offset:         40
        .size:           4
        .value_kind:     by_value
      - .actual_access:  read_only
        .address_space:  global
        .offset:         48
        .size:           8
        .value_kind:     global_buffer
    .group_segment_fixed_size: 0
    .kernarg_segment_align: 8
    .kernarg_segment_size: 56
    .language:       OpenCL C
    .language_version:
      - 2
      - 0
    .max_flat_workgroup_size: 512
    .name:           _Z9tg_kernelILi64ELi8ELi1ELb0EEvPKDF16_iS1_iPviPKf
    .private_segment_fixed_size: 0
    .sgpr_count:     26
    .sgpr_spill_count: 0
    .symbol:         _Z9tg_kernelILi64ELi8ELi1ELb0EEvPKDF16_iS1_iPviPKf.kd
    .uniform_work_group_size: 1
    .uses_dynamic_stack: false
    .vgpr_count:     62
    .vgpr_spill_count: 0
    .wavefront_size: 64
  - .agpr_count:     0
    .args:
      - .address_space:  global
        .offset:         0
        .size:           8
        .value_kind:     global_buffer
      - .offset:         8
        .size:           4
        .value_kind:     by_value
      - .address_space:  global
        .offset:         16
        .size:           8
        .value_kind:     global_buffer
      - .offset:         24
        .size:           4
        .value_kind:     by_value
      - .actual_access:  write_only
        .address_space:  global
        .offset:         32
        .size:           8
        .value_kind:     global_buffer
      - .offset:         40
        .size:           4
        .value_kind:     by_value
      - .actual_access:  read_only
        .address_space:  global
        .offset:         48
        .size:           8
        .value_kind:     global_buffer
    .group_segment_fixed_size: 0
    .kernarg_segment_align: 8
    .kernarg_segment_size: 56
    .language:       OpenCL C
    .language_version:
      - 2
      - 0
    .max_flat_workgroup_size: 512
    .name:           _Z9tg_kernelILi64ELi8ELi4ELb0EEvPKDF16_iS1_iPviPKf
    .private_segment_fixed_size: 0
    .sgpr_count:     26
    .sgpr_spill_count: 0
    .symbol:         _Z9tg_kernelILi64ELi8ELi4ELb0EEvPKDF16_iS1_iPviPKf.kd
    .uniform_work_group_size: 1
    .uses_dynamic_stack: false
    .vgpr_count:     64
    .vgpr_spill_count: 0
    .wavefront_size: 64
  - .agpr_count:     0
    .args:
      - .address_space:  global
        .offset:         0
        .size:           8
        .value_kind:     global_buffer
      - .offset:         8
        .size:           4
        .value_kind:     by_value
      - .address_space:  global
        .offset:         16
        .size:           8
        .value_kind:     global_buffer
      - .offset:         24
        .size:           4
        .value_kind:     by_value
      - .actual_access:  write_only
        .address_space:  global
        .offset:         32
        .size:           8
        .value_kind:     global_buffer
      - .offset:         40
        .size:           4
        .value_kind:     by_value
      - .actual_access:  read_only
        .address_space:  global
        .offset:         48
        .size:           8
        .value_kind:     global_buffer
    .group_segment_fixed_size: 0
    .kernarg_segment_align: 8
    .kernarg_segment_size: 56
    .language:       OpenCL C
    .language_version:
      - 2
      - 0
    .max_flat_workgroup_size: 512
    .name:           _Z9tg_kernelILi64ELi8ELi2ELb0EEvPKDF16_iS1_iPviPKf
    .private_segment_fixed_size: 0
    .sgpr_count:     22
    .sgpr_spill_count: 0
    .symbol:         _Z9tg_kernelILi64ELi8ELi2ELb0EEvPKDF16_iS1_iPviPKf.kd
    .uniform_work_group_size: 1
    .uses_dynamic_stack: false
    .vgpr_count:     62
    .vgpr_spill_count: 0
    .wavefront_size: 64
